# baseline (speedup 1.0000x reference)
.Lbc_scan:
	v_lshlrev_b32_e32 v1, 3, v0
	ds_read_b64 v[8:9], v1
	s_waitcnt lgkmcnt(0)
	v_add_u32_e32 v10, v8, v9
	v_mov_b32_e32 v11, v10
	s_nop 1
	v_add_u32_dpp v11, v11, v11 row_shr:1 row_mask:0xf bank_mask:0xf bound_ctrl:0
	s_nop 1
	v_add_u32_dpp v11, v11, v11 row_shr:2 row_mask:0xf bank_mask:0xf bound_ctrl:0
	s_nop 1
	v_add_u32_dpp v11, v11, v11 row_shr:4 row_mask:0xf bank_mask:0xf bound_ctrl:0
	s_nop 1
	v_add_u32_dpp v11, v11, v11 row_shr:8 row_mask:0xf bank_mask:0xf bound_ctrl:0
	s_nop 1
	v_add_u32_dpp v11, v11, v11 row_bcast:15 row_mask:0xa bank_mask:0xf
	s_nop 1
	v_add_u32_dpp v11, v11, v11 row_bcast:31 row_mask:0xc bank_mask:0xf
	v_lshrrev_b32_e32 v12, 6, v0
	s_nop 0
	v_readfirstlane_b32 s3, v12
	v_readlane_b32 s16, v11, 63
	s_lshl_b32 s17, s3, 2
	s_add_u32 s17, s17, 0x1020
	v_mov_b32_e32 v12, s16
	v_mov_b32_e32 v13, s17
	s_mov_b64 s[32:33], exec
	s_mov_b64 exec, 1
	ds_write_b32 v13, v12
	v_mov_b32_e32 v14, s21
	v_mov_b32_e32 v15, 0x1000
	ds_write_b32 v15, v14
	s_mov_b64 exec, s[32:33]
	s_waitcnt lgkmcnt(0)
	s_barrier
	v_mov_b32_e32 v13, 0x1020
	ds_read_b128 v[12:15], v13
	v_mov_b32_e32 v2, 0
	s_waitcnt lgkmcnt(0)
	s_cmp_gt_u32 s3, 0
	s_cselect_b32 s16, 1, 0
	v_mad_u32_u24 v2, v12, s16, v2
	s_cmp_gt_u32 s3, 1
	s_cselect_b32 s16, 1, 0
	v_mad_u32_u24 v2, v13, s16, v2
	s_cmp_gt_u32 s3, 2
	s_cselect_b32 s16, 1, 0
	v_mad_u32_u24 v2, v14, s16, v2
	v_sub_u32_e32 v4, v11, v10
	v_add_u32_e32 v4, v4, v2
	v_add_u32_e32 v5, v4, v8
	ds_write_b64 v1, v[4:5] offset:2048
	v_add_u32_e32 v6, s14, v4
	v_add_u32_e32 v7, s14, v5
	v_lshlrev_b32_e32 v12, 1, v0
	v_add_lshl_u32 v13, v12, s20, 2
	v_cmp_gt_u32_e32 vcc, s22, v12
	s_and_saveexec_b64 s[32:33], vcc
	s_cbranch_execz .Lbc_nooff
	global_store_dwordx2 v13, v[6:7], s[8:9]

.Lbc_pl:
	s_mov_b64 exec, -1
	s_waitcnt vmcnt(0) lgkmcnt(0)
	s_barrier
	s_cmp_ge_u32 s20, 0x61a80
	s_cbranch_scc1 .Lpl_end
	v_lshlrev_b32_e32 v1, 3, v0
	ds_read_b64 v[4:5], v1 offset:2048
	ds_read_b32 v6, v1 offset:2056
	v_mov_b32_e32 v7, s21
	v_cmp_eq_u32_e32 vcc, 0xff, v0
	s_waitcnt lgkmcnt(0)
	s_nop 1
	v_cndmask_b32_e32 v6, v6, v7, vcc
	v_sub_u32_e32 v8, v5, v4
	v_sub_u32_e32 v9, v6, v5
	v_max_u32_e32 v10, v8, v9
	s_nop 1
	v_max_u32_dpp v10, v10, v10 quad_perm:[1,0,3,2] row_mask:0xf bank_mask:0xf
	s_nop 1
	v_max_u32_dpp v10, v10, v10 quad_perm:[2,3,0,1] row_mask:0xf bank_mask:0xf
	s_nop 1
	v_max_u32_dpp v10, v10, v10 row_half_mirror row_mask:0xf bank_mask:0xf
	v_lshrrev_b32_e32 v11, 3, v0
	s_lshr_b32 s0, s20, 4
	v_add_u32_e32 v11, s0, v11
	s_movk_i32 s1, 0x61a8
	v_cmp_gt_u32_e64 s[2:3], s1, v11
	s_add_u32 s24, s10, 0x712bd00
	s_addc_u32 s25, s11, 0
	s_add_u32 s16, s24, 0x186a000
	s_addc_u32 s17, s25, 0
	v_and_b32_e32 v12, 7, v0
	v_cmp_eq_u32_e32 vcc, 0, v12
	s_and_b64 s[18:19], vcc, s[2:3]
	v_lshlrev_b32_e32 v22, 2, v11
	s_and_saveexec_b64 s[12:13], s[18:19]
	s_cbranch_execz .Lpl_nom
	global_store_dword v22, v10, s[16:17]

.Lbc_pl2:
	s_cmp_ge_u32 s20, 0x61a80
	s_cbranch_scc1 .Lp2_end
	v_lshrrev_b32_e32 v1, 3, v0
	v_and_b32_e32 v2, 3, v0
	v_bfe_u32 v3, v0, 2, 1
	v_lshl_add_u32 v4, v1, 2, v2
	v_lshlrev_b32_e32 v4, 4, v4
	ds_read_b128 v[8:11], v4 offset:2048
	ds_read_b32 v12, v4 offset:2064
	s_lshr_b32 s0, s20, 4
	v_add_u32_e32 v5, s0, v1
	s_movk_i32 s1, 0x61a8
	v_cmp_gt_u32_e64 s[2:3], s1, v5
	s_add_u32 s24, s10, 0x712bd00
	s_addc_u32 s25, s11, 0
	s_add_u32 s16, s24, 0x186a000
	s_addc_u32 s17, s25, 0
	s_waitcnt lgkmcnt(0)
	v_sub_u32_e32 v13, v9, v8
	v_sub_u32_e32 v14, v10, v9
	v_sub_u32_e32 v15, v11, v10
	v_sub_u32_e32 v16, v12, v11
	v_max_u32_e32 v17, v13, v14
	v_max3_u32 v17, v17, v15, v16
	s_nop 1
	v_max_u32_dpp v17, v17, v17 quad_perm:[1,0,3,2] row_mask:0xf bank_mask:0xf
	s_nop 1
	v_max_u32_dpp v17, v17, v17 quad_perm:[2,3,0,1] row_mask:0xf bank_mask:0xf
	v_and_b32_e32 v18, 7, v0
	v_cmp_eq_u32_e32 vcc, 0, v18
	s_and_b64 s[18:19], vcc, s[2:3]
	v_lshlrev_b32_e32 v19, 2, v5
	s_and_saveexec_b64 s[12:13], s[18:19]
	s_cbranch_execz .Lp2_nom
	global_store_dword v19, v17, s[16:17]
.Lp2_nom:
	s_mov_b64 exec, s[12:13]
	v_add_u32_e32 v20, 1, v17
	v_and_b32_e32 v20, -2, v20
	v_min_u32_e32 v20, 16, v20
	v_lshlrev_b32_e32 v21, 10, v5
	v_lshl_add_u32 v21, v2, 4, v21
	v_lshl_add_u32 v21, v3, 6, v21
	v_add_lshl_u32 v8, v8, v3, 2
	v_add_lshl_u32 v9, v9, v3, 2
	v_add_lshl_u32 v10, v10, v3, 2
	v_add_lshl_u32 v11, v11, v3, 2
	v_mov_b32_e32 v22, v3
	v_mov_b32_e32 v23, 0x800000
	s_and_b64 exec, exec, s[2:3]
	s_cbranch_execz .Lp2_end
.Lp2_loop:
	v_cmp_lt_u32_e32 vcc, v22, v20
	s_and_b64 exec, exec, vcc
	s_cbranch_execz .Lp2_end
	ds_read_b32 v24, v8 offset:4352
	ds_read_b32 v25, v9 offset:4352
	ds_read_b32 v26, v10 offset:4352
	ds_read_b32 v27, v11 offset:4352
	s_waitcnt lgkmcnt(0)
	v_cmp_lt_u32_e32 vcc, v22, v13
	v_add_u32_e32 v8, 8, v8
	v_add_u32_e32 v9, 8, v9
	v_cndmask_b32_e32 v24, v23, v24, vcc
	v_cmp_lt_u32_e32 vcc, v22, v14
	v_add_u32_e32 v10, 8, v10
	v_add_u32_e32 v11, 8, v11
	v_cndmask_b32_e32 v25, v23, v25, vcc
	v_cmp_lt_u32_e32 vcc, v22, v15
	s_nop 1
	v_cndmask_b32_e32 v26, v23, v26, vcc
	v_cmp_lt_u32_e32 vcc, v22, v16
	v_add_u32_e32 v22, 2, v22
	s_nop 0
	v_cndmask_b32_e32 v27, v23, v27, vcc
	s_nop 0
	global_store_dwordx4 v21, v[24:27], s[24:25]
	v_add_u32_e32 v21, 0x80, v21
	s_branch .Lp2_loop
